# W4 plus: up/down K-loop LDS-DMA loads use scalar-base + 32-bit offset addressing (64 v_lshl_add_u64 removed from the load segments)
# baseline (speedup 1.0000x reference)
.LBB0_1172:
	s_ashr_i32 s39, s38, 31
	s_lshl_b64 s[4:5], s[38:39], 20
	s_add_u32 s40, s18, s4
	s_addc_u32 s41, s19, s5
	s_and_b64 s[4:5], s[36:37], exec
	s_cselect_b32 s4, s41, s1
	s_cselect_b32 s5, s40, s0
	s_ashr_i32 s35, s34, 31
	s_lshl_b64 s[42:43], s[34:35], 20
	s_add_u32 s42, s16, s42
	s_addc_u32 s43, s17, s43
	s_and_b64 s[48:49], s[36:37], exec
	s_cselect_b32 s35, s43, s47
	s_cselect_b32 s39, s42, s46
	s_add_u32 s76, s46, 0x10000
	s_addc_u32 s77, s47, 0
	s_mov_b32 s78, -2
	v_add_u32_e32 v124, s28, v156
	v_add_u32_e32 v170, s45, v156
	ds_read_b128 v[108:111], v124
	ds_read_b128 v[112:115], v124 offset:1024
	ds_read_b128 v[120:123], v124 offset:2048
	ds_read_b128 v[124:127], v124 offset:3072
	ds_read_b128 v[158:161], v170
	ds_read_b128 v[162:165], v170 offset:1024
	ds_read_b128 v[166:169], v170 offset:2048
	ds_read_b128 v[170:173], v170 offset:3072
	ds_read_b128 v[174:177], v157
	ds_read_b128 v[178:181], v157 offset:1024
	ds_read_b128 v[182:185], v157 offset:2048
	ds_read_b128 v[186:189], v157 offset:3072
	ds_read_b128 v[190:193], v157 offset:4096
	ds_read_b128 v[194:197], v157 offset:5120
	ds_read_b128 v[198:201], v157 offset:6144
	ds_read_b128 v[202:205], v157 offset:7168
	s_add_u32 s46, s0, 0x10000
	s_addc_u32 s47, s1, 0
	s_cmp_eq_u32 s78, 28
	s_cselect_b32 s52, s5, s46
	s_cselect_b32 s53, s4, s47
	s_cselect_b32 s50, s39, s76
	s_cselect_b32 s51, s35, s77
	s_add_u32 s48, s52, 0x8000
	s_addc_u32 s49, s53, 0
	s_add_i32 m0, s56, 0xc000
	s_nop 0
	global_load_lds_dwordx4 v152, s[0:1]
	s_add_i32 m0, s56, 0xe000
	s_nop 0
	global_load_lds_dwordx4 v154, s[0:1]
	s_waitcnt vmcnt(8)
	s_waitcnt lgkmcnt(0)
	s_setprio 1
	s_barrier
	v_mfma_f32_16x16x32_bf16 v[140:143], v[108:111], v[174:177], 0
	v_mfma_f32_16x16x32_bf16 v[136:139], v[120:123], v[174:177], 0
	v_mfma_f32_16x16x32_bf16 v[116:119], v[108:111], v[182:185], 0
	v_mfma_f32_16x16x32_bf16 v[104:107], v[120:123], v[182:185], 0
	v_mfma_f32_16x16x32_bf16 v[92:95], v[108:111], v[190:193], 0
	v_mfma_f32_16x16x32_bf16 v[88:91], v[120:123], v[190:193], 0
	v_mfma_f32_16x16x32_bf16 v[76:79], v[108:111], v[198:201], 0
	v_mfma_f32_16x16x32_bf16 v[72:75], v[120:123], v[198:201], 0
	v_mfma_f32_16x16x32_bf16 v[140:143], v[112:115], v[178:181], v[140:143]
	v_mfma_f32_16x16x32_bf16 v[136:139], v[124:127], v[178:181], v[136:139]
	v_mfma_f32_16x16x32_bf16 v[116:119], v[112:115], v[186:189], v[116:119]
	v_mfma_f32_16x16x32_bf16 v[104:107], v[124:127], v[186:189], v[104:107]
	v_mfma_f32_16x16x32_bf16 v[92:95], v[112:115], v[194:197], v[92:95]
	v_mfma_f32_16x16x32_bf16 v[88:91], v[124:127], v[194:197], v[88:91]
	v_mfma_f32_16x16x32_bf16 v[76:79], v[112:115], v[202:205], v[76:79]
	v_mfma_f32_16x16x32_bf16 v[72:75], v[124:127], v[202:205], v[72:75]
	s_setprio 0
	s_setprio 1
	v_mfma_f32_16x16x32_bf16 v[132:135], v[158:161], v[174:177], 0
	v_mfma_f32_16x16x32_bf16 v[128:131], v[166:169], v[174:177], 0
	v_mfma_f32_16x16x32_bf16 v[100:103], v[158:161], v[182:185], 0
	v_mfma_f32_16x16x32_bf16 v[96:99], v[166:169], v[182:185], 0
	v_mfma_f32_16x16x32_bf16 v[84:87], v[158:161], v[190:193], 0
	v_mfma_f32_16x16x32_bf16 v[80:83], v[166:169], v[190:193], 0
	v_mfma_f32_16x16x32_bf16 v[68:71], v[158:161], v[198:201], 0
	v_mfma_f32_16x16x32_bf16 v[64:67], v[166:169], v[198:201], 0
	v_mfma_f32_16x16x32_bf16 v[132:135], v[162:165], v[178:181], v[132:135]
	v_mfma_f32_16x16x32_bf16 v[128:131], v[170:173], v[178:181], v[128:131]
	v_mfma_f32_16x16x32_bf16 v[100:103], v[162:165], v[186:189], v[100:103]
	v_mfma_f32_16x16x32_bf16 v[96:99], v[170:173], v[186:189], v[96:99]
	v_mfma_f32_16x16x32_bf16 v[84:87], v[162:165], v[194:197], v[84:87]
	v_mfma_f32_16x16x32_bf16 v[80:83], v[170:173], v[194:197], v[80:83]
	v_mfma_f32_16x16x32_bf16 v[68:71], v[162:165], v[202:205], v[68:71]
	v_mfma_f32_16x16x32_bf16 v[64:67], v[170:173], v[202:205], v[64:67]
	s_barrier
	s_setprio 0
	ds_read_b128 v[174:177], v157 offset:16384
	ds_read_b128 v[178:181], v157 offset:17408
	ds_read_b128 v[182:185], v157 offset:18432
	ds_read_b128 v[186:189], v157 offset:19456
	ds_read_b128 v[190:193], v157 offset:20480
	ds_read_b128 v[194:197], v157 offset:21504
	ds_read_b128 v[198:201], v157 offset:22528
	ds_read_b128 v[202:205], v157 offset:23552
	s_mov_b32 m0, s30
	s_add_u32 s0, s50, 0x4000
	global_load_lds_dwordx4 v146, s[50:51]
	s_mov_b32 m0, s31
	s_addc_u32 s1, s51, 0
	global_load_lds_dwordx4 v150, s[50:51]
	s_mov_b32 m0, s54
	s_nop 0
	global_load_lds_dwordx4 v146, s[0:1]
	s_mov_b32 m0, s55
	s_nop 0
	global_load_lds_dwordx4 v150, s[0:1]
	s_mov_b32 m0, s56
	s_nop 0
	global_load_lds_dwordx4 v144, s[52:53]
	s_mov_b32 m0, s57
	s_nop 0
	global_load_lds_dwordx4 v148, s[52:53]
	s_waitcnt vmcnt(8)
	s_waitcnt lgkmcnt(0)
	s_setprio 1
	s_barrier
	v_mfma_f32_16x16x32_bf16 v[60:63], v[108:111], v[174:177], 0
	v_mfma_f32_16x16x32_bf16 v[56:59], v[120:123], v[174:177], 0
	v_mfma_f32_16x16x32_bf16 v[44:47], v[108:111], v[182:185], 0
	v_mfma_f32_16x16x32_bf16 v[40:43], v[120:123], v[182:185], 0
	v_mfma_f32_16x16x32_bf16 v[28:31], v[108:111], v[190:193], 0
	v_mfma_f32_16x16x32_bf16 v[24:27], v[120:123], v[190:193], 0
	v_mfma_f32_16x16x32_bf16 v[12:15], v[108:111], v[198:201], 0
	v_mfma_f32_16x16x32_bf16 v[8:11], v[120:123], v[198:201], 0
	v_mfma_f32_16x16x32_bf16 v[60:63], v[112:115], v[178:181], v[60:63]
	v_mfma_f32_16x16x32_bf16 v[56:59], v[124:127], v[178:181], v[56:59]
	v_mfma_f32_16x16x32_bf16 v[44:47], v[112:115], v[186:189], v[44:47]
	v_mfma_f32_16x16x32_bf16 v[40:43], v[124:127], v[186:189], v[40:43]
	v_mfma_f32_16x16x32_bf16 v[28:31], v[112:115], v[194:197], v[28:31]
	v_mfma_f32_16x16x32_bf16 v[24:27], v[124:127], v[194:197], v[24:27]
	v_mfma_f32_16x16x32_bf16 v[12:15], v[112:115], v[202:205], v[12:15]
	v_mfma_f32_16x16x32_bf16 v[8:11], v[124:127], v[202:205], v[8:11]
	s_setprio 0
	s_setprio 1
	v_mfma_f32_16x16x32_bf16 v[52:55], v[158:161], v[174:177], 0
	v_mfma_f32_16x16x32_bf16 v[48:51], v[166:169], v[174:177], 0
	v_mfma_f32_16x16x32_bf16 v[36:39], v[158:161], v[182:185], 0
	v_mfma_f32_16x16x32_bf16 v[32:35], v[166:169], v[182:185], 0
	v_mfma_f32_16x16x32_bf16 v[20:23], v[158:161], v[190:193], 0
	v_mfma_f32_16x16x32_bf16 v[16:19], v[166:169], v[190:193], 0
	v_mfma_f32_16x16x32_bf16 v[4:7], v[158:161], v[198:201], 0
	v_mfma_f32_16x16x32_bf16 v[0:3], v[166:169], v[198:201], 0
	v_mfma_f32_16x16x32_bf16 v[52:55], v[162:165], v[178:181], v[52:55]
	v_mfma_f32_16x16x32_bf16 v[48:51], v[170:173], v[178:181], v[48:51]
	v_mfma_f32_16x16x32_bf16 v[36:39], v[162:165], v[186:189], v[36:39]
	v_mfma_f32_16x16x32_bf16 v[32:35], v[170:173], v[186:189], v[32:35]
	v_mfma_f32_16x16x32_bf16 v[20:23], v[162:165], v[194:197], v[20:23]
	v_mfma_f32_16x16x32_bf16 v[16:19], v[170:173], v[194:197], v[16:19]
	v_mfma_f32_16x16x32_bf16 v[4:7], v[162:165], v[202:205], v[4:7]
	v_mfma_f32_16x16x32_bf16 v[0:3], v[170:173], v[202:205], v[0:3]
	s_barrier
	s_setprio 0
	v_add_u32_e32 v124, s62, v156
	v_add_u32_e32 v170, s67, v156
	ds_read_b128 v[108:111], v124
	ds_read_b128 v[112:115], v124 offset:1024
	ds_read_b128 v[120:123], v124 offset:2048
	ds_read_b128 v[124:127], v124 offset:3072
	ds_read_b128 v[158:161], v170
	ds_read_b128 v[162:165], v170 offset:1024
	ds_read_b128 v[166:169], v170 offset:2048
	ds_read_b128 v[170:173], v170 offset:3072
	ds_read_b128 v[174:177], v157 offset:32768
	ds_read_b128 v[178:181], v157 offset:33792
	ds_read_b128 v[182:185], v157 offset:34816
	ds_read_b128 v[186:189], v157 offset:35840
	ds_read_b128 v[190:193], v157 offset:36864
	ds_read_b128 v[194:197], v157 offset:37888
	ds_read_b128 v[198:201], v157 offset:38912
	ds_read_b128 v[202:205], v157 offset:39936
	s_add_u32 s0, s52, 0x4000
	s_addc_u32 s1, s53, 0
	s_mov_b32 m0, s58
	s_nop 0
	global_load_lds_dwordx4 v144, s[0:1]
	s_mov_b32 m0, s59
	s_nop 0
	global_load_lds_dwordx4 v148, s[0:1]
	s_waitcnt vmcnt(8)
	s_waitcnt lgkmcnt(0)
	s_setprio 1
	s_barrier
	v_mfma_f32_16x16x32_bf16 v[140:143], v[108:111], v[174:177], v[140:143]
	v_mfma_f32_16x16x32_bf16 v[136:139], v[120:123], v[174:177], v[136:139]
	v_mfma_f32_16x16x32_bf16 v[116:119], v[108:111], v[182:185], v[116:119]
	v_mfma_f32_16x16x32_bf16 v[104:107], v[120:123], v[182:185], v[104:107]
	v_mfma_f32_16x16x32_bf16 v[92:95], v[108:111], v[190:193], v[92:95]
	v_mfma_f32_16x16x32_bf16 v[88:91], v[120:123], v[190:193], v[88:91]
	v_mfma_f32_16x16x32_bf16 v[76:79], v[108:111], v[198:201], v[76:79]
	v_mfma_f32_16x16x32_bf16 v[72:75], v[120:123], v[198:201], v[72:75]
	v_mfma_f32_16x16x32_bf16 v[140:143], v[112:115], v[178:181], v[140:143]
	v_mfma_f32_16x16x32_bf16 v[136:139], v[124:127], v[178:181], v[136:139]
	v_mfma_f32_16x16x32_bf16 v[116:119], v[112:115], v[186:189], v[116:119]
	v_mfma_f32_16x16x32_bf16 v[104:107], v[124:127], v[186:189], v[104:107]
	v_mfma_f32_16x16x32_bf16 v[92:95], v[112:115], v[194:197], v[92:95]
	v_mfma_f32_16x16x32_bf16 v[88:91], v[124:127], v[194:197], v[88:91]
	v_mfma_f32_16x16x32_bf16 v[76:79], v[112:115], v[202:205], v[76:79]
	v_mfma_f32_16x16x32_bf16 v[72:75], v[124:127], v[202:205], v[72:75]
	s_setprio 0
	s_setprio 1
	v_mfma_f32_16x16x32_bf16 v[132:135], v[158:161], v[174:177], v[132:135]
	v_mfma_f32_16x16x32_bf16 v[128:131], v[166:169], v[174:177], v[128:131]
	v_mfma_f32_16x16x32_bf16 v[100:103], v[158:161], v[182:185], v[100:103]
	v_mfma_f32_16x16x32_bf16 v[96:99], v[166:169], v[182:185], v[96:99]
	v_mfma_f32_16x16x32_bf16 v[84:87], v[158:161], v[190:193], v[84:87]
	v_mfma_f32_16x16x32_bf16 v[80:83], v[166:169], v[190:193], v[80:83]
	v_mfma_f32_16x16x32_bf16 v[68:71], v[158:161], v[198:201], v[68:71]
	v_mfma_f32_16x16x32_bf16 v[64:67], v[166:169], v[198:201], v[64:67]
	v_mfma_f32_16x16x32_bf16 v[132:135], v[162:165], v[178:181], v[132:135]
	v_mfma_f32_16x16x32_bf16 v[128:131], v[170:173], v[178:181], v[128:131]
	v_mfma_f32_16x16x32_bf16 v[100:103], v[162:165], v[186:189], v[100:103]
	v_mfma_f32_16x16x32_bf16 v[96:99], v[170:173], v[186:189], v[96:99]
	v_mfma_f32_16x16x32_bf16 v[84:87], v[162:165], v[194:197], v[84:87]
	v_mfma_f32_16x16x32_bf16 v[80:83], v[170:173], v[194:197], v[80:83]
	v_mfma_f32_16x16x32_bf16 v[68:71], v[162:165], v[202:205], v[68:71]
	v_mfma_f32_16x16x32_bf16 v[64:67], v[170:173], v[202:205], v[64:67]
	s_barrier
	s_setprio 0
	ds_read_b128 v[174:177], v157 offset:49152
	ds_read_b128 v[178:181], v157 offset:50176
	ds_read_b128 v[182:185], v157 offset:51200
	ds_read_b128 v[186:189], v157 offset:52224
	ds_read_b128 v[190:193], v157 offset:53248
	ds_read_b128 v[194:197], v157 offset:54272
	ds_read_b128 v[198:201], v157 offset:55296
	ds_read_b128 v[202:205], v157 offset:56320
	s_add_u32 s0, s50, 0x8000
	s_addc_u32 s1, s51, 0
	s_mov_b32 m0, s63
	s_nop 0
	global_load_lds_dwordx4 v146, s[0:1]
	s_mov_b32 m0, s64
	s_nop 0
	global_load_lds_dwordx4 v150, s[0:1]
	s_add_u32 s0, s50, 0xc000
	s_addc_u32 s1, s51, 0
	s_mov_b32 m0, s68
	s_nop 0
	global_load_lds_dwordx4 v146, s[0:1]
	s_mov_b32 m0, s69
	s_nop 0
	global_load_lds_dwordx4 v150, s[0:1]
	s_mov_b32 m0, s65
	s_nop 0
	global_load_lds_dwordx4 v144, s[48:49]
	s_mov_b32 m0, s66
	s_nop 0
	global_load_lds_dwordx4 v148, s[48:49]
	s_waitcnt vmcnt(8)
	s_waitcnt lgkmcnt(0)
	s_setprio 1
	s_barrier
	v_mfma_f32_16x16x32_bf16 v[60:63], v[108:111], v[174:177], v[60:63]
	v_mfma_f32_16x16x32_bf16 v[56:59], v[120:123], v[174:177], v[56:59]
	v_mfma_f32_16x16x32_bf16 v[44:47], v[108:111], v[182:185], v[44:47]
	v_mfma_f32_16x16x32_bf16 v[40:43], v[120:123], v[182:185], v[40:43]
	v_mfma_f32_16x16x32_bf16 v[28:31], v[108:111], v[190:193], v[28:31]
	v_mfma_f32_16x16x32_bf16 v[24:27], v[120:123], v[190:193], v[24:27]
	v_mfma_f32_16x16x32_bf16 v[12:15], v[108:111], v[198:201], v[12:15]
	v_mfma_f32_16x16x32_bf16 v[8:11], v[120:123], v[198:201], v[8:11]
	v_mfma_f32_16x16x32_bf16 v[60:63], v[112:115], v[178:181], v[60:63]
	v_mfma_f32_16x16x32_bf16 v[56:59], v[124:127], v[178:181], v[56:59]
	v_mfma_f32_16x16x32_bf16 v[44:47], v[112:115], v[186:189], v[44:47]
	v_mfma_f32_16x16x32_bf16 v[40:43], v[124:127], v[186:189], v[40:43]
	v_mfma_f32_16x16x32_bf16 v[28:31], v[112:115], v[194:197], v[28:31]
	v_mfma_f32_16x16x32_bf16 v[24:27], v[124:127], v[194:197], v[24:27]
	v_mfma_f32_16x16x32_bf16 v[12:15], v[112:115], v[202:205], v[12:15]
	v_mfma_f32_16x16x32_bf16 v[8:11], v[124:127], v[202:205], v[8:11]
	s_setprio 0
	s_setprio 1
	v_mfma_f32_16x16x32_bf16 v[52:55], v[158:161], v[174:177], v[52:55]
	v_mfma_f32_16x16x32_bf16 v[48:51], v[166:169], v[174:177], v[48:51]
	v_mfma_f32_16x16x32_bf16 v[36:39], v[158:161], v[182:185], v[36:39]
	v_mfma_f32_16x16x32_bf16 v[32:35], v[166:169], v[182:185], v[32:35]
	v_mfma_f32_16x16x32_bf16 v[20:23], v[158:161], v[190:193], v[20:23]
	v_mfma_f32_16x16x32_bf16 v[16:19], v[166:169], v[190:193], v[16:19]
	v_mfma_f32_16x16x32_bf16 v[4:7], v[158:161], v[198:201], v[4:7]
	v_mfma_f32_16x16x32_bf16 v[0:3], v[166:169], v[198:201], v[0:3]
	v_mfma_f32_16x16x32_bf16 v[52:55], v[162:165], v[178:181], v[52:55]
	v_mfma_f32_16x16x32_bf16 v[48:51], v[170:173], v[178:181], v[48:51]
	v_mfma_f32_16x16x32_bf16 v[36:39], v[162:165], v[186:189], v[36:39]
	v_mfma_f32_16x16x32_bf16 v[32:35], v[170:173], v[186:189], v[32:35]
	v_mfma_f32_16x16x32_bf16 v[20:23], v[162:165], v[194:197], v[20:23]
	v_mfma_f32_16x16x32_bf16 v[16:19], v[170:173], v[194:197], v[16:19]
	v_mfma_f32_16x16x32_bf16 v[4:7], v[162:165], v[202:205], v[4:7]
	v_mfma_f32_16x16x32_bf16 v[0:3], v[170:173], v[202:205], v[0:3]
	s_barrier
	s_setprio 0
	s_add_i32 s78, s78, 2
	s_add_u32 s76, s76, 0x10000
	s_addc_u32 s77, s77, 0
	s_cmp_gt_u32 s78, 29
	s_mov_b64 s[0:1], s[46:47]
.LBB0_1173:
	v_add_u32_e32 v124, s28, v156
	v_add_u32_e32 v170, s45, v156
	ds_read_b128 v[108:111], v124
	ds_read_b128 v[112:115], v124 offset:1024
	ds_read_b128 v[120:123], v124 offset:2048
	ds_read_b128 v[124:127], v124 offset:3072
	ds_read_b128 v[158:161], v170
	ds_read_b128 v[162:165], v170 offset:1024
	ds_read_b128 v[166:169], v170 offset:2048
	ds_read_b128 v[170:173], v170 offset:3072
	ds_read_b128 v[174:177], v157
	ds_read_b128 v[178:181], v157 offset:1024
	ds_read_b128 v[182:185], v157 offset:2048
	ds_read_b128 v[186:189], v157 offset:3072
	ds_read_b128 v[190:193], v157 offset:4096
	ds_read_b128 v[194:197], v157 offset:5120
	ds_read_b128 v[198:201], v157 offset:6144
	ds_read_b128 v[202:205], v157 offset:7168
	s_add_u32 s46, s0, 0x10000
	s_addc_u32 s47, s1, 0
	s_cmp_eq_u32 s78, 28
	s_cselect_b32 s52, s5, s46
	s_cselect_b32 s53, s4, s47
	s_cselect_b32 s50, s39, s76
	s_cselect_b32 s51, s35, s77
	s_add_u32 s48, s52, 0x8000
	s_addc_u32 s49, s53, 0
	s_add_i32 m0, s56, 0xc000
	s_nop 0
	global_load_lds_dwordx4 v152, s[0:1]
	s_add_i32 m0, s56, 0xe000
	s_nop 0
	global_load_lds_dwordx4 v154, s[0:1]
	s_waitcnt vmcnt(8)
	s_waitcnt lgkmcnt(0)
	s_setprio 1
	s_barrier
	v_mfma_f32_16x16x32_bf16 v[140:143], v[108:111], v[174:177], v[140:143]
	v_mfma_f32_16x16x32_bf16 v[136:139], v[120:123], v[174:177], v[136:139]
	v_mfma_f32_16x16x32_bf16 v[116:119], v[108:111], v[182:185], v[116:119]
	v_mfma_f32_16x16x32_bf16 v[104:107], v[120:123], v[182:185], v[104:107]
	v_mfma_f32_16x16x32_bf16 v[92:95], v[108:111], v[190:193], v[92:95]
	v_mfma_f32_16x16x32_bf16 v[88:91], v[120:123], v[190:193], v[88:91]
	v_mfma_f32_16x16x32_bf16 v[76:79], v[108:111], v[198:201], v[76:79]
	v_mfma_f32_16x16x32_bf16 v[72:75], v[120:123], v[198:201], v[72:75]
	v_mfma_f32_16x16x32_bf16 v[140:143], v[112:115], v[178:181], v[140:143]
	v_mfma_f32_16x16x32_bf16 v[136:139], v[124:127], v[178:181], v[136:139]
	v_mfma_f32_16x16x32_bf16 v[116:119], v[112:115], v[186:189], v[116:119]
	v_mfma_f32_16x16x32_bf16 v[104:107], v[124:127], v[186:189], v[104:107]
	v_mfma_f32_16x16x32_bf16 v[92:95], v[112:115], v[194:197], v[92:95]
	v_mfma_f32_16x16x32_bf16 v[88:91], v[124:127], v[194:197], v[88:91]
	v_mfma_f32_16x16x32_bf16 v[76:79], v[112:115], v[202:205], v[76:79]
	v_mfma_f32_16x16x32_bf16 v[72:75], v[124:127], v[202:205], v[72:75]
	s_setprio 0
	s_setprio 1
	v_mfma_f32_16x16x32_bf16 v[132:135], v[158:161], v[174:177], v[132:135]
	v_mfma_f32_16x16x32_bf16 v[128:131], v[166:169], v[174:177], v[128:131]
	v_mfma_f32_16x16x32_bf16 v[100:103], v[158:161], v[182:185], v[100:103]
	v_mfma_f32_16x16x32_bf16 v[96:99], v[166:169], v[182:185], v[96:99]
	v_mfma_f32_16x16x32_bf16 v[84:87], v[158:161], v[190:193], v[84:87]
	v_mfma_f32_16x16x32_bf16 v[80:83], v[166:169], v[190:193], v[80:83]
	v_mfma_f32_16x16x32_bf16 v[68:71], v[158:161], v[198:201], v[68:71]
	v_mfma_f32_16x16x32_bf16 v[64:67], v[166:169], v[198:201], v[64:67]
	v_mfma_f32_16x16x32_bf16 v[132:135], v[162:165], v[178:181], v[132:135]
	v_mfma_f32_16x16x32_bf16 v[128:131], v[170:173], v[178:181], v[128:131]
	v_mfma_f32_16x16x32_bf16 v[100:103], v[162:165], v[186:189], v[100:103]
	v_mfma_f32_16x16x32_bf16 v[96:99], v[170:173], v[186:189], v[96:99]
	v_mfma_f32_16x16x32_bf16 v[84:87], v[162:165], v[194:197], v[84:87]
	v_mfma_f32_16x16x32_bf16 v[80:83], v[170:173], v[194:197], v[80:83]
	v_mfma_f32_16x16x32_bf16 v[68:71], v[162:165], v[202:205], v[68:71]
	v_mfma_f32_16x16x32_bf16 v[64:67], v[170:173], v[202:205], v[64:67]
	s_barrier
	s_setprio 0
	ds_read_b128 v[174:177], v157 offset:16384
	ds_read_b128 v[178:181], v157 offset:17408
	ds_read_b128 v[182:185], v157 offset:18432
	ds_read_b128 v[186:189], v157 offset:19456
	ds_read_b128 v[190:193], v157 offset:20480
	ds_read_b128 v[194:197], v157 offset:21504
	ds_read_b128 v[198:201], v157 offset:22528
	ds_read_b128 v[202:205], v157 offset:23552
	s_mov_b32 m0, s30
	s_add_u32 s0, s50, 0x4000
	global_load_lds_dwordx4 v146, s[50:51]
	s_mov_b32 m0, s31
	s_addc_u32 s1, s51, 0
	global_load_lds_dwordx4 v150, s[50:51]
	s_mov_b32 m0, s54
	s_nop 0
	global_load_lds_dwordx4 v146, s[0:1]
	s_mov_b32 m0, s55
	s_nop 0
	global_load_lds_dwordx4 v150, s[0:1]
	s_mov_b32 m0, s56
	s_nop 0
	global_load_lds_dwordx4 v144, s[52:53]
	s_mov_b32 m0, s57
	s_nop 0
	global_load_lds_dwordx4 v148, s[52:53]
	s_waitcnt vmcnt(8)
	s_waitcnt lgkmcnt(0)
	s_setprio 1
	s_barrier
	v_mfma_f32_16x16x32_bf16 v[60:63], v[108:111], v[174:177], v[60:63]
	v_mfma_f32_16x16x32_bf16 v[56:59], v[120:123], v[174:177], v[56:59]
	v_mfma_f32_16x16x32_bf16 v[44:47], v[108:111], v[182:185], v[44:47]
	v_mfma_f32_16x16x32_bf16 v[40:43], v[120:123], v[182:185], v[40:43]
	v_mfma_f32_16x16x32_bf16 v[28:31], v[108:111], v[190:193], v[28:31]
	v_mfma_f32_16x16x32_bf16 v[24:27], v[120:123], v[190:193], v[24:27]
	v_mfma_f32_16x16x32_bf16 v[12:15], v[108:111], v[198:201], v[12:15]
	v_mfma_f32_16x16x32_bf16 v[8:11], v[120:123], v[198:201], v[8:11]
	v_mfma_f32_16x16x32_bf16 v[60:63], v[112:115], v[178:181], v[60:63]
	v_mfma_f32_16x16x32_bf16 v[56:59], v[124:127], v[178:181], v[56:59]
	v_mfma_f32_16x16x32_bf16 v[44:47], v[112:115], v[186:189], v[44:47]
	v_mfma_f32_16x16x32_bf16 v[40:43], v[124:127], v[186:189], v[40:43]
	v_mfma_f32_16x16x32_bf16 v[28:31], v[112:115], v[194:197], v[28:31]
	v_mfma_f32_16x16x32_bf16 v[24:27], v[124:127], v[194:197], v[24:27]
	v_mfma_f32_16x16x32_bf16 v[12:15], v[112:115], v[202:205], v[12:15]
	v_mfma_f32_16x16x32_bf16 v[8:11], v[124:127], v[202:205], v[8:11]
	s_setprio 0
	s_setprio 1
	v_mfma_f32_16x16x32_bf16 v[52:55], v[158:161], v[174:177], v[52:55]
	v_mfma_f32_16x16x32_bf16 v[48:51], v[166:169], v[174:177], v[48:51]
	v_mfma_f32_16x16x32_bf16 v[36:39], v[158:161], v[182:185], v[36:39]
	v_mfma_f32_16x16x32_bf16 v[32:35], v[166:169], v[182:185], v[32:35]
	v_mfma_f32_16x16x32_bf16 v[20:23], v[158:161], v[190:193], v[20:23]
	v_mfma_f32_16x16x32_bf16 v[16:19], v[166:169], v[190:193], v[16:19]
	v_mfma_f32_16x16x32_bf16 v[4:7], v[158:161], v[198:201], v[4:7]
	v_mfma_f32_16x16x32_bf16 v[0:3], v[166:169], v[198:201], v[0:3]
	v_mfma_f32_16x16x32_bf16 v[52:55], v[162:165], v[178:181], v[52:55]
	v_mfma_f32_16x16x32_bf16 v[48:51], v[170:173], v[178:181], v[48:51]
	v_mfma_f32_16x16x32_bf16 v[36:39], v[162:165], v[186:189], v[36:39]
	v_mfma_f32_16x16x32_bf16 v[32:35], v[170:173], v[186:189], v[32:35]
	v_mfma_f32_16x16x32_bf16 v[20:23], v[162:165], v[194:197], v[20:23]
	v_mfma_f32_16x16x32_bf16 v[16:19], v[170:173], v[194:197], v[16:19]
	v_mfma_f32_16x16x32_bf16 v[4:7], v[162:165], v[202:205], v[4:7]
	v_mfma_f32_16x16x32_bf16 v[0:3], v[170:173], v[202:205], v[0:3]
	s_barrier
	s_setprio 0
	v_add_u32_e32 v124, s62, v156
	v_add_u32_e32 v170, s67, v156
	ds_read_b128 v[108:111], v124
	ds_read_b128 v[112:115], v124 offset:1024
	ds_read_b128 v[120:123], v124 offset:2048
	ds_read_b128 v[124:127], v124 offset:3072
	ds_read_b128 v[158:161], v170
	ds_read_b128 v[162:165], v170 offset:1024
	ds_read_b128 v[166:169], v170 offset:2048
	ds_read_b128 v[170:173], v170 offset:3072
	ds_read_b128 v[174:177], v157 offset:32768
	ds_read_b128 v[178:181], v157 offset:33792
	ds_read_b128 v[182:185], v157 offset:34816
	ds_read_b128 v[186:189], v157 offset:35840
	ds_read_b128 v[190:193], v157 offset:36864
	ds_read_b128 v[194:197], v157 offset:37888
	ds_read_b128 v[198:201], v157 offset:38912
	ds_read_b128 v[202:205], v157 offset:39936
	s_add_u32 s0, s52, 0x4000
	s_addc_u32 s1, s53, 0
	s_mov_b32 m0, s58
	s_nop 0
	global_load_lds_dwordx4 v144, s[0:1]
	s_mov_b32 m0, s59
	s_nop 0
	global_load_lds_dwordx4 v148, s[0:1]
	s_waitcnt vmcnt(8)
	s_waitcnt lgkmcnt(0)
	s_setprio 1
	s_barrier
	v_mfma_f32_16x16x32_bf16 v[140:143], v[108:111], v[174:177], v[140:143]
	v_mfma_f32_16x16x32_bf16 v[136:139], v[120:123], v[174:177], v[136:139]
	v_mfma_f32_16x16x32_bf16 v[116:119], v[108:111], v[182:185], v[116:119]
	v_mfma_f32_16x16x32_bf16 v[104:107], v[120:123], v[182:185], v[104:107]
	v_mfma_f32_16x16x32_bf16 v[92:95], v[108:111], v[190:193], v[92:95]
	v_mfma_f32_16x16x32_bf16 v[88:91], v[120:123], v[190:193], v[88:91]
	v_mfma_f32_16x16x32_bf16 v[76:79], v[108:111], v[198:201], v[76:79]
	v_mfma_f32_16x16x32_bf16 v[72:75], v[120:123], v[198:201], v[72:75]
	v_mfma_f32_16x16x32_bf16 v[140:143], v[112:115], v[178:181], v[140:143]
	v_mfma_f32_16x16x32_bf16 v[136:139], v[124:127], v[178:181], v[136:139]
	v_mfma_f32_16x16x32_bf16 v[116:119], v[112:115], v[186:189], v[116:119]
	v_mfma_f32_16x16x32_bf16 v[104:107], v[124:127], v[186:189], v[104:107]
	v_mfma_f32_16x16x32_bf16 v[92:95], v[112:115], v[194:197], v[92:95]
	v_mfma_f32_16x16x32_bf16 v[88:91], v[124:127], v[194:197], v[88:91]
	v_mfma_f32_16x16x32_bf16 v[76:79], v[112:115], v[202:205], v[76:79]
	v_mfma_f32_16x16x32_bf16 v[72:75], v[124:127], v[202:205], v[72:75]
	s_setprio 0
	s_setprio 1
	v_mfma_f32_16x16x32_bf16 v[132:135], v[158:161], v[174:177], v[132:135]
	v_mfma_f32_16x16x32_bf16 v[128:131], v[166:169], v[174:177], v[128:131]
	v_mfma_f32_16x16x32_bf16 v[100:103], v[158:161], v[182:185], v[100:103]
	v_mfma_f32_16x16x32_bf16 v[96:99], v[166:169], v[182:185], v[96:99]
	v_mfma_f32_16x16x32_bf16 v[84:87], v[158:161], v[190:193], v[84:87]
	v_mfma_f32_16x16x32_bf16 v[80:83], v[166:169], v[190:193], v[80:83]
	v_mfma_f32_16x16x32_bf16 v[68:71], v[158:161], v[198:201], v[68:71]
	v_mfma_f32_16x16x32_bf16 v[64:67], v[166:169], v[198:201], v[64:67]
	v_mfma_f32_16x16x32_bf16 v[132:135], v[162:165], v[178:181], v[132:135]
	v_mfma_f32_16x16x32_bf16 v[128:131], v[170:173], v[178:181], v[128:131]
	v_mfma_f32_16x16x32_bf16 v[100:103], v[162:165], v[186:189], v[100:103]
	v_mfma_f32_16x16x32_bf16 v[96:99], v[170:173], v[186:189], v[96:99]
	v_mfma_f32_16x16x32_bf16 v[84:87], v[162:165], v[194:197], v[84:87]
	v_mfma_f32_16x16x32_bf16 v[80:83], v[170:173], v[194:197], v[80:83]
	v_mfma_f32_16x16x32_bf16 v[68:71], v[162:165], v[202:205], v[68:71]
	v_mfma_f32_16x16x32_bf16 v[64:67], v[170:173], v[202:205], v[64:67]
	s_barrier
	s_setprio 0
	ds_read_b128 v[174:177], v157 offset:49152
	ds_read_b128 v[178:181], v157 offset:50176
	ds_read_b128 v[182:185], v157 offset:51200
	ds_read_b128 v[186:189], v157 offset:52224
	ds_read_b128 v[190:193], v157 offset:53248
	ds_read_b128 v[194:197], v157 offset:54272
	ds_read_b128 v[198:201], v157 offset:55296
	ds_read_b128 v[202:205], v157 offset:56320
	s_add_u32 s0, s50, 0x8000
	s_addc_u32 s1, s51, 0
	s_mov_b32 m0, s63
	s_nop 0
	global_load_lds_dwordx4 v146, s[0:1]
	s_mov_b32 m0, s64
	s_nop 0
	global_load_lds_dwordx4 v150, s[0:1]
	s_add_u32 s0, s50, 0xc000
	s_addc_u32 s1, s51, 0
	s_mov_b32 m0, s68
	s_nop 0
	global_load_lds_dwordx4 v146, s[0:1]
	s_mov_b32 m0, s69
	s_nop 0
	global_load_lds_dwordx4 v150, s[0:1]
	s_mov_b32 m0, s65
	s_nop 0
	global_load_lds_dwordx4 v144, s[48:49]
	s_mov_b32 m0, s66
	s_nop 0
	global_load_lds_dwordx4 v148, s[48:49]
	s_waitcnt vmcnt(8)
	s_waitcnt lgkmcnt(0)
	s_setprio 1
	s_barrier
	v_mfma_f32_16x16x32_bf16 v[60:63], v[108:111], v[174:177], v[60:63]
	v_mfma_f32_16x16x32_bf16 v[56:59], v[120:123], v[174:177], v[56:59]
	v_mfma_f32_16x16x32_bf16 v[44:47], v[108:111], v[182:185], v[44:47]
	v_mfma_f32_16x16x32_bf16 v[40:43], v[120:123], v[182:185], v[40:43]
	v_mfma_f32_16x16x32_bf16 v[28:31], v[108:111], v[190:193], v[28:31]
	v_mfma_f32_16x16x32_bf16 v[24:27], v[120:123], v[190:193], v[24:27]
	v_mfma_f32_16x16x32_bf16 v[12:15], v[108:111], v[198:201], v[12:15]
	v_mfma_f32_16x16x32_bf16 v[8:11], v[120:123], v[198:201], v[8:11]
	v_mfma_f32_16x16x32_bf16 v[60:63], v[112:115], v[178:181], v[60:63]
	v_mfma_f32_16x16x32_bf16 v[56:59], v[124:127], v[178:181], v[56:59]
	v_mfma_f32_16x16x32_bf16 v[44:47], v[112:115], v[186:189], v[44:47]
	v_mfma_f32_16x16x32_bf16 v[40:43], v[124:127], v[186:189], v[40:43]
	v_mfma_f32_16x16x32_bf16 v[28:31], v[112:115], v[194:197], v[28:31]
	v_mfma_f32_16x16x32_bf16 v[24:27], v[124:127], v[194:197], v[24:27]
	v_mfma_f32_16x16x32_bf16 v[12:15], v[112:115], v[202:205], v[12:15]
	v_mfma_f32_16x16x32_bf16 v[8:11], v[124:127], v[202:205], v[8:11]
	s_setprio 0
	s_setprio 1
	v_mfma_f32_16x16x32_bf16 v[52:55], v[158:161], v[174:177], v[52:55]
	v_mfma_f32_16x16x32_bf16 v[48:51], v[166:169], v[174:177], v[48:51]
	v_mfma_f32_16x16x32_bf16 v[36:39], v[158:161], v[182:185], v[36:39]
	v_mfma_f32_16x16x32_bf16 v[32:35], v[166:169], v[182:185], v[32:35]
	v_mfma_f32_16x16x32_bf16 v[20:23], v[158:161], v[190:193], v[20:23]
	v_mfma_f32_16x16x32_bf16 v[16:19], v[166:169], v[190:193], v[16:19]
	v_mfma_f32_16x16x32_bf16 v[4:7], v[158:161], v[198:201], v[4:7]
	v_mfma_f32_16x16x32_bf16 v[0:3], v[166:169], v[198:201], v[0:3]
	v_mfma_f32_16x16x32_bf16 v[52:55], v[162:165], v[178:181], v[52:55]
	v_mfma_f32_16x16x32_bf16 v[48:51], v[170:173], v[178:181], v[48:51]
	v_mfma_f32_16x16x32_bf16 v[36:39], v[162:165], v[186:189], v[36:39]
	v_mfma_f32_16x16x32_bf16 v[32:35], v[170:173], v[186:189], v[32:35]
	v_mfma_f32_16x16x32_bf16 v[20:23], v[162:165], v[194:197], v[20:23]
	v_mfma_f32_16x16x32_bf16 v[16:19], v[170:173], v[194:197], v[16:19]
	v_mfma_f32_16x16x32_bf16 v[4:7], v[162:165], v[202:205], v[4:7]
	v_mfma_f32_16x16x32_bf16 v[0:3], v[170:173], v[202:205], v[0:3]
	s_barrier
	s_setprio 0
	s_add_i32 s78, s78, 2
	s_add_u32 s76, s76, 0x10000
	s_addc_u32 s77, s77, 0
	s_cmp_gt_u32 s78, 29
	s_mov_b64 s[0:1], s[46:47]
	s_cbranch_scc0 .LBB0_1173
	s_and_b64 vcc, exec, s[24:25]
	s_cbranch_vccz .LBB0_1176
	s_barrier

.LBB0_1247:
	s_ashr_i32 s35, s34, 31
	s_lshl_b64 s[4:5], s[34:35], 22
	s_add_u32 s38, s17, s4
	s_addc_u32 s39, s18, s5
	s_and_b64 s[4:5], s[36:37], exec
	s_cselect_b32 s4, s39, s1
	s_cselect_b32 s5, s38, s0
	s_ashr_i32 s25, s24, 31
	s_lshl_b64 s[40:41], s[24:25], 22
	s_add_u32 s40, s19, s40
	s_addc_u32 s41, s28, s41
	s_and_b64 s[46:47], s[36:37], exec
	s_cselect_b32 s25, s41, s45
	s_cselect_b32 s35, s40, s44
	s_add_u32 s74, s44, 0x10000
	s_addc_u32 s75, s45, 0
	s_mov_b32 s76, -2
	v_add_u32_e32 v92, s30, v206
	v_add_u32_e32 v156, s52, v206
	ds_read_b128 v[72:75], v92
	ds_read_b128 v[76:79], v92 offset:1024
	ds_read_b128 v[84:87], v92 offset:2048
	ds_read_b128 v[92:95], v92 offset:3072
	ds_read_b128 v[144:147], v156
	ds_read_b128 v[148:151], v156 offset:1024
	ds_read_b128 v[152:155], v156 offset:2048
	ds_read_b128 v[156:159], v156 offset:3072
	ds_read_b128 v[160:163], v207
	ds_read_b128 v[164:167], v207 offset:1024
	ds_read_b128 v[168:171], v207 offset:2048
	ds_read_b128 v[184:187], v207 offset:3072
	ds_read_b128 v[188:191], v207 offset:4096
	ds_read_b128 v[192:195], v207 offset:5120
	ds_read_b128 v[196:199], v207 offset:6144
	ds_read_b128 v[200:203], v207 offset:7168
	s_add_u32 s44, s0, 0x10000
	s_addc_u32 s45, s1, 0
	s_cmpk_eq_i32 s76, 0x7c
	s_cselect_b32 s50, s5, s44
	s_cselect_b32 s51, s4, s45
	s_cselect_b32 s48, s35, s74
	s_cselect_b32 s49, s25, s75
	s_add_u32 s46, s50, 0x8000
	s_addc_u32 s47, s51, 0
	s_add_i32 m0, s56, 0xc000
	s_nop 0
	global_load_lds_dwordx4 v180, s[0:1]
	s_add_i32 m0, s56, 0xe000
	s_nop 0
	global_load_lds_dwordx4 v182, s[0:1]
	s_waitcnt vmcnt(8)
	s_waitcnt lgkmcnt(0)
	s_setprio 1
	s_barrier
	v_mfma_f32_16x16x32_bf16 v[140:143], v[72:75], v[160:163], 0
	v_mfma_f32_16x16x32_bf16 v[136:139], v[84:87], v[160:163], 0
	v_mfma_f32_16x16x32_bf16 v[124:127], v[72:75], v[168:171], 0
	v_mfma_f32_16x16x32_bf16 v[120:123], v[84:87], v[168:171], 0
	v_mfma_f32_16x16x32_bf16 v[108:111], v[72:75], v[188:191], 0
	v_mfma_f32_16x16x32_bf16 v[104:107], v[84:87], v[188:191], 0
	v_mfma_f32_16x16x32_bf16 v[88:91], v[72:75], v[196:199], 0
	v_mfma_f32_16x16x32_bf16 v[80:83], v[84:87], v[196:199], 0
	v_mfma_f32_16x16x32_bf16 v[140:143], v[76:79], v[164:167], v[140:143]
	v_mfma_f32_16x16x32_bf16 v[136:139], v[92:95], v[164:167], v[136:139]
	v_mfma_f32_16x16x32_bf16 v[124:127], v[76:79], v[184:187], v[124:127]
	v_mfma_f32_16x16x32_bf16 v[120:123], v[92:95], v[184:187], v[120:123]
	v_mfma_f32_16x16x32_bf16 v[108:111], v[76:79], v[192:195], v[108:111]
	v_mfma_f32_16x16x32_bf16 v[104:107], v[92:95], v[192:195], v[104:107]
	v_mfma_f32_16x16x32_bf16 v[88:91], v[76:79], v[200:203], v[88:91]
	v_mfma_f32_16x16x32_bf16 v[80:83], v[92:95], v[200:203], v[80:83]
	s_setprio 0
	s_setprio 1
	v_mfma_f32_16x16x32_bf16 v[132:135], v[144:147], v[160:163], 0
	v_mfma_f32_16x16x32_bf16 v[128:131], v[152:155], v[160:163], 0
	v_mfma_f32_16x16x32_bf16 v[116:119], v[144:147], v[168:171], 0
	v_mfma_f32_16x16x32_bf16 v[112:115], v[152:155], v[168:171], 0
	v_mfma_f32_16x16x32_bf16 v[100:103], v[144:147], v[188:191], 0
	v_mfma_f32_16x16x32_bf16 v[96:99], v[152:155], v[188:191], 0
	v_mfma_f32_16x16x32_bf16 v[68:71], v[144:147], v[196:199], 0
	v_mfma_f32_16x16x32_bf16 v[64:67], v[152:155], v[196:199], 0
	v_mfma_f32_16x16x32_bf16 v[132:135], v[148:151], v[164:167], v[132:135]
	v_mfma_f32_16x16x32_bf16 v[128:131], v[156:159], v[164:167], v[128:131]
	v_mfma_f32_16x16x32_bf16 v[116:119], v[148:151], v[184:187], v[116:119]
	v_mfma_f32_16x16x32_bf16 v[112:115], v[156:159], v[184:187], v[112:115]
	v_mfma_f32_16x16x32_bf16 v[100:103], v[148:151], v[192:195], v[100:103]
	v_mfma_f32_16x16x32_bf16 v[96:99], v[156:159], v[192:195], v[96:99]
	v_mfma_f32_16x16x32_bf16 v[68:71], v[148:151], v[200:203], v[68:71]
	v_mfma_f32_16x16x32_bf16 v[64:67], v[156:159], v[200:203], v[64:67]
	s_barrier
	s_setprio 0
	ds_read_b128 v[160:163], v207 offset:16384
	ds_read_b128 v[164:167], v207 offset:17408
	ds_read_b128 v[168:171], v207 offset:18432
	ds_read_b128 v[184:187], v207 offset:19456
	ds_read_b128 v[188:191], v207 offset:20480
	ds_read_b128 v[192:195], v207 offset:21504
	ds_read_b128 v[196:199], v207 offset:22528
	ds_read_b128 v[200:203], v207 offset:23552
	s_mov_b32 m0, s31
	s_add_u32 s0, s48, 0x4000
	global_load_lds_dwordx4 v174, s[48:49]
	s_mov_b32 m0, s43
	s_addc_u32 s1, s49, 0
	global_load_lds_dwordx4 v178, s[48:49]
	s_mov_b32 m0, s53
	s_nop 0
	global_load_lds_dwordx4 v174, s[0:1]
	s_mov_b32 m0, s54
	s_nop 0
	global_load_lds_dwordx4 v178, s[0:1]
	s_mov_b32 m0, s56
	s_nop 0
	global_load_lds_dwordx4 v172, s[50:51]
	s_mov_b32 m0, s57
	s_nop 0
	global_load_lds_dwordx4 v176, s[50:51]
	s_waitcnt vmcnt(8)
	s_waitcnt lgkmcnt(0)
	s_setprio 1
	s_barrier
	v_mfma_f32_16x16x32_bf16 v[60:63], v[72:75], v[160:163], 0
	v_mfma_f32_16x16x32_bf16 v[56:59], v[84:87], v[160:163], 0
	v_mfma_f32_16x16x32_bf16 v[44:47], v[72:75], v[168:171], 0
	v_mfma_f32_16x16x32_bf16 v[40:43], v[84:87], v[168:171], 0
	v_mfma_f32_16x16x32_bf16 v[28:31], v[72:75], v[188:191], 0
	v_mfma_f32_16x16x32_bf16 v[24:27], v[84:87], v[188:191], 0
	v_mfma_f32_16x16x32_bf16 v[12:15], v[72:75], v[196:199], 0
	v_mfma_f32_16x16x32_bf16 v[8:11], v[84:87], v[196:199], 0
	v_mfma_f32_16x16x32_bf16 v[60:63], v[76:79], v[164:167], v[60:63]
	v_mfma_f32_16x16x32_bf16 v[56:59], v[92:95], v[164:167], v[56:59]
	v_mfma_f32_16x16x32_bf16 v[44:47], v[76:79], v[184:187], v[44:47]
	v_mfma_f32_16x16x32_bf16 v[40:43], v[92:95], v[184:187], v[40:43]
	v_mfma_f32_16x16x32_bf16 v[28:31], v[76:79], v[192:195], v[28:31]
	v_mfma_f32_16x16x32_bf16 v[24:27], v[92:95], v[192:195], v[24:27]
	v_mfma_f32_16x16x32_bf16 v[12:15], v[76:79], v[200:203], v[12:15]
	v_mfma_f32_16x16x32_bf16 v[8:11], v[92:95], v[200:203], v[8:11]
	s_setprio 0
	s_setprio 1
	v_mfma_f32_16x16x32_bf16 v[52:55], v[144:147], v[160:163], 0
	v_mfma_f32_16x16x32_bf16 v[48:51], v[152:155], v[160:163], 0
	v_mfma_f32_16x16x32_bf16 v[36:39], v[144:147], v[168:171], 0
	v_mfma_f32_16x16x32_bf16 v[32:35], v[152:155], v[168:171], 0
	v_mfma_f32_16x16x32_bf16 v[20:23], v[144:147], v[188:191], 0
	v_mfma_f32_16x16x32_bf16 v[16:19], v[152:155], v[188:191], 0
	v_mfma_f32_16x16x32_bf16 v[4:7], v[144:147], v[196:199], 0
	v_mfma_f32_16x16x32_bf16 v[0:3], v[152:155], v[196:199], 0
	v_mfma_f32_16x16x32_bf16 v[52:55], v[148:151], v[164:167], v[52:55]
	v_mfma_f32_16x16x32_bf16 v[48:51], v[156:159], v[164:167], v[48:51]
	v_mfma_f32_16x16x32_bf16 v[36:39], v[148:151], v[184:187], v[36:39]
	v_mfma_f32_16x16x32_bf16 v[32:35], v[156:159], v[184:187], v[32:35]
	v_mfma_f32_16x16x32_bf16 v[20:23], v[148:151], v[192:195], v[20:23]
	v_mfma_f32_16x16x32_bf16 v[16:19], v[156:159], v[192:195], v[16:19]
	v_mfma_f32_16x16x32_bf16 v[4:7], v[148:151], v[200:203], v[4:7]
	v_mfma_f32_16x16x32_bf16 v[0:3], v[156:159], v[200:203], v[0:3]
	s_barrier
	s_setprio 0
	v_add_u32_e32 v92, s64, v206
	v_add_u32_e32 v156, s69, v206
	ds_read_b128 v[72:75], v92
	ds_read_b128 v[76:79], v92 offset:1024
	ds_read_b128 v[84:87], v92 offset:2048
	ds_read_b128 v[92:95], v92 offset:3072
	ds_read_b128 v[144:147], v156
	ds_read_b128 v[148:151], v156 offset:1024
	ds_read_b128 v[152:155], v156 offset:2048
	ds_read_b128 v[156:159], v156 offset:3072
	ds_read_b128 v[160:163], v207 offset:32768
	ds_read_b128 v[164:167], v207 offset:33792
	ds_read_b128 v[168:171], v207 offset:34816
	ds_read_b128 v[184:187], v207 offset:35840
	ds_read_b128 v[188:191], v207 offset:36864
	ds_read_b128 v[192:195], v207 offset:37888
	ds_read_b128 v[196:199], v207 offset:38912
	ds_read_b128 v[200:203], v207 offset:39936
	s_add_u32 s0, s50, 0x4000
	s_addc_u32 s1, s51, 0
	s_mov_b32 m0, s58
	s_nop 0
	global_load_lds_dwordx4 v172, s[0:1]
	s_mov_b32 m0, s59
	s_nop 0
	global_load_lds_dwordx4 v176, s[0:1]
	s_waitcnt vmcnt(8)
	s_waitcnt lgkmcnt(0)
	s_setprio 1
	s_barrier
	v_mfma_f32_16x16x32_bf16 v[140:143], v[72:75], v[160:163], v[140:143]
	v_mfma_f32_16x16x32_bf16 v[136:139], v[84:87], v[160:163], v[136:139]
	v_mfma_f32_16x16x32_bf16 v[124:127], v[72:75], v[168:171], v[124:127]
	v_mfma_f32_16x16x32_bf16 v[120:123], v[84:87], v[168:171], v[120:123]
	v_mfma_f32_16x16x32_bf16 v[108:111], v[72:75], v[188:191], v[108:111]
	v_mfma_f32_16x16x32_bf16 v[104:107], v[84:87], v[188:191], v[104:107]
	v_mfma_f32_16x16x32_bf16 v[88:91], v[72:75], v[196:199], v[88:91]
	v_mfma_f32_16x16x32_bf16 v[80:83], v[84:87], v[196:199], v[80:83]
	v_mfma_f32_16x16x32_bf16 v[140:143], v[76:79], v[164:167], v[140:143]
	v_mfma_f32_16x16x32_bf16 v[136:139], v[92:95], v[164:167], v[136:139]
	v_mfma_f32_16x16x32_bf16 v[124:127], v[76:79], v[184:187], v[124:127]
	v_mfma_f32_16x16x32_bf16 v[120:123], v[92:95], v[184:187], v[120:123]
	v_mfma_f32_16x16x32_bf16 v[108:111], v[76:79], v[192:195], v[108:111]
	v_mfma_f32_16x16x32_bf16 v[104:107], v[92:95], v[192:195], v[104:107]
	v_mfma_f32_16x16x32_bf16 v[88:91], v[76:79], v[200:203], v[88:91]
	v_mfma_f32_16x16x32_bf16 v[80:83], v[92:95], v[200:203], v[80:83]
	s_setprio 0
	s_setprio 1
	v_mfma_f32_16x16x32_bf16 v[132:135], v[144:147], v[160:163], v[132:135]
	v_mfma_f32_16x16x32_bf16 v[128:131], v[152:155], v[160:163], v[128:131]
	v_mfma_f32_16x16x32_bf16 v[116:119], v[144:147], v[168:171], v[116:119]
	v_mfma_f32_16x16x32_bf16 v[112:115], v[152:155], v[168:171], v[112:115]
	v_mfma_f32_16x16x32_bf16 v[100:103], v[144:147], v[188:191], v[100:103]
	v_mfma_f32_16x16x32_bf16 v[96:99], v[152:155], v[188:191], v[96:99]
	v_mfma_f32_16x16x32_bf16 v[68:71], v[144:147], v[196:199], v[68:71]
	v_mfma_f32_16x16x32_bf16 v[64:67], v[152:155], v[196:199], v[64:67]
	v_mfma_f32_16x16x32_bf16 v[132:135], v[148:151], v[164:167], v[132:135]
	v_mfma_f32_16x16x32_bf16 v[128:131], v[156:159], v[164:167], v[128:131]
	v_mfma_f32_16x16x32_bf16 v[116:119], v[148:151], v[184:187], v[116:119]
	v_mfma_f32_16x16x32_bf16 v[112:115], v[156:159], v[184:187], v[112:115]
	v_mfma_f32_16x16x32_bf16 v[100:103], v[148:151], v[192:195], v[100:103]
	v_mfma_f32_16x16x32_bf16 v[96:99], v[156:159], v[192:195], v[96:99]
	v_mfma_f32_16x16x32_bf16 v[68:71], v[148:151], v[200:203], v[68:71]
	v_mfma_f32_16x16x32_bf16 v[64:67], v[156:159], v[200:203], v[64:67]
	s_barrier
	s_setprio 0
	ds_read_b128 v[160:163], v207 offset:49152
	ds_read_b128 v[164:167], v207 offset:50176
	ds_read_b128 v[168:171], v207 offset:51200
	ds_read_b128 v[184:187], v207 offset:52224
	ds_read_b128 v[188:191], v207 offset:53248
	ds_read_b128 v[192:195], v207 offset:54272
	ds_read_b128 v[196:199], v207 offset:55296
	ds_read_b128 v[200:203], v207 offset:56320
	s_add_u32 s0, s48, 0x8000
	s_addc_u32 s1, s49, 0
	s_mov_b32 m0, s65
	s_nop 0
	global_load_lds_dwordx4 v174, s[0:1]
	s_mov_b32 m0, s66
	s_nop 0
	global_load_lds_dwordx4 v178, s[0:1]
	s_add_u32 s0, s48, 0xc000
	s_addc_u32 s1, s49, 0
	s_mov_b32 m0, s70
	s_nop 0
	global_load_lds_dwordx4 v174, s[0:1]
	s_mov_b32 m0, s71
	s_nop 0
	global_load_lds_dwordx4 v178, s[0:1]
	s_mov_b32 m0, s67
	s_nop 0
	global_load_lds_dwordx4 v172, s[46:47]
	s_mov_b32 m0, s68
	s_nop 0
	global_load_lds_dwordx4 v176, s[46:47]
	s_waitcnt vmcnt(8)
	s_waitcnt lgkmcnt(0)
	s_setprio 1
	s_barrier
	v_mfma_f32_16x16x32_bf16 v[60:63], v[72:75], v[160:163], v[60:63]
	v_mfma_f32_16x16x32_bf16 v[56:59], v[84:87], v[160:163], v[56:59]
	v_mfma_f32_16x16x32_bf16 v[44:47], v[72:75], v[168:171], v[44:47]
	v_mfma_f32_16x16x32_bf16 v[40:43], v[84:87], v[168:171], v[40:43]
	v_mfma_f32_16x16x32_bf16 v[28:31], v[72:75], v[188:191], v[28:31]
	v_mfma_f32_16x16x32_bf16 v[24:27], v[84:87], v[188:191], v[24:27]
	v_mfma_f32_16x16x32_bf16 v[12:15], v[72:75], v[196:199], v[12:15]
	v_mfma_f32_16x16x32_bf16 v[8:11], v[84:87], v[196:199], v[8:11]
	v_mfma_f32_16x16x32_bf16 v[60:63], v[76:79], v[164:167], v[60:63]
	v_mfma_f32_16x16x32_bf16 v[56:59], v[92:95], v[164:167], v[56:59]
	v_mfma_f32_16x16x32_bf16 v[44:47], v[76:79], v[184:187], v[44:47]
	v_mfma_f32_16x16x32_bf16 v[40:43], v[92:95], v[184:187], v[40:43]
	v_mfma_f32_16x16x32_bf16 v[28:31], v[76:79], v[192:195], v[28:31]
	v_mfma_f32_16x16x32_bf16 v[24:27], v[92:95], v[192:195], v[24:27]
	v_mfma_f32_16x16x32_bf16 v[12:15], v[76:79], v[200:203], v[12:15]
	v_mfma_f32_16x16x32_bf16 v[8:11], v[92:95], v[200:203], v[8:11]
	s_setprio 0
	s_setprio 1
	v_mfma_f32_16x16x32_bf16 v[52:55], v[144:147], v[160:163], v[52:55]
	v_mfma_f32_16x16x32_bf16 v[48:51], v[152:155], v[160:163], v[48:51]
	v_mfma_f32_16x16x32_bf16 v[36:39], v[144:147], v[168:171], v[36:39]
	v_mfma_f32_16x16x32_bf16 v[32:35], v[152:155], v[168:171], v[32:35]
	v_mfma_f32_16x16x32_bf16 v[20:23], v[144:147], v[188:191], v[20:23]
	v_mfma_f32_16x16x32_bf16 v[16:19], v[152:155], v[188:191], v[16:19]
	v_mfma_f32_16x16x32_bf16 v[4:7], v[144:147], v[196:199], v[4:7]
	v_mfma_f32_16x16x32_bf16 v[0:3], v[152:155], v[196:199], v[0:3]
	v_mfma_f32_16x16x32_bf16 v[52:55], v[148:151], v[164:167], v[52:55]
	v_mfma_f32_16x16x32_bf16 v[48:51], v[156:159], v[164:167], v[48:51]
	v_mfma_f32_16x16x32_bf16 v[36:39], v[148:151], v[184:187], v[36:39]
	v_mfma_f32_16x16x32_bf16 v[32:35], v[156:159], v[184:187], v[32:35]
	v_mfma_f32_16x16x32_bf16 v[20:23], v[148:151], v[192:195], v[20:23]
	v_mfma_f32_16x16x32_bf16 v[16:19], v[156:159], v[192:195], v[16:19]
	v_mfma_f32_16x16x32_bf16 v[4:7], v[148:151], v[200:203], v[4:7]
	v_mfma_f32_16x16x32_bf16 v[0:3], v[156:159], v[200:203], v[0:3]
	s_barrier
	s_setprio 0
	s_add_i32 s76, s76, 2
	s_add_u32 s74, s74, 0x10000
	s_addc_u32 s75, s75, 0
	s_cmpk_gt_u32 s76, 0x7d
	s_mov_b64 s[0:1], s[44:45]
.LBB0_1248:
	v_add_u32_e32 v92, s30, v206
	v_add_u32_e32 v156, s52, v206
	ds_read_b128 v[72:75], v92
	ds_read_b128 v[76:79], v92 offset:1024
	ds_read_b128 v[84:87], v92 offset:2048
	ds_read_b128 v[92:95], v92 offset:3072
	ds_read_b128 v[144:147], v156
	ds_read_b128 v[148:151], v156 offset:1024
	ds_read_b128 v[152:155], v156 offset:2048
	ds_read_b128 v[156:159], v156 offset:3072
	ds_read_b128 v[160:163], v207
	ds_read_b128 v[164:167], v207 offset:1024
	ds_read_b128 v[168:171], v207 offset:2048
	ds_read_b128 v[184:187], v207 offset:3072
	ds_read_b128 v[188:191], v207 offset:4096
	ds_read_b128 v[192:195], v207 offset:5120
	ds_read_b128 v[196:199], v207 offset:6144
	ds_read_b128 v[200:203], v207 offset:7168
	s_add_u32 s44, s0, 0x10000
	s_addc_u32 s45, s1, 0
	s_cmpk_eq_i32 s76, 0x7c
	s_cselect_b32 s50, s5, s44
	s_cselect_b32 s51, s4, s45
	s_cselect_b32 s48, s35, s74
	s_cselect_b32 s49, s25, s75
	s_add_u32 s46, s50, 0x8000
	s_addc_u32 s47, s51, 0
	s_add_i32 m0, s56, 0xc000
	s_nop 0
	global_load_lds_dwordx4 v180, s[0:1]
	s_add_i32 m0, s56, 0xe000
	s_nop 0
	global_load_lds_dwordx4 v182, s[0:1]
	s_waitcnt vmcnt(8)
	s_waitcnt lgkmcnt(0)
	s_setprio 1
	s_barrier
	v_mfma_f32_16x16x32_bf16 v[140:143], v[72:75], v[160:163], v[140:143]
	v_mfma_f32_16x16x32_bf16 v[136:139], v[84:87], v[160:163], v[136:139]
	v_mfma_f32_16x16x32_bf16 v[124:127], v[72:75], v[168:171], v[124:127]
	v_mfma_f32_16x16x32_bf16 v[120:123], v[84:87], v[168:171], v[120:123]
	v_mfma_f32_16x16x32_bf16 v[108:111], v[72:75], v[188:191], v[108:111]
	v_mfma_f32_16x16x32_bf16 v[104:107], v[84:87], v[188:191], v[104:107]
	v_mfma_f32_16x16x32_bf16 v[88:91], v[72:75], v[196:199], v[88:91]
	v_mfma_f32_16x16x32_bf16 v[80:83], v[84:87], v[196:199], v[80:83]
	v_mfma_f32_16x16x32_bf16 v[140:143], v[76:79], v[164:167], v[140:143]
	v_mfma_f32_16x16x32_bf16 v[136:139], v[92:95], v[164:167], v[136:139]
	v_mfma_f32_16x16x32_bf16 v[124:127], v[76:79], v[184:187], v[124:127]
	v_mfma_f32_16x16x32_bf16 v[120:123], v[92:95], v[184:187], v[120:123]
	v_mfma_f32_16x16x32_bf16 v[108:111], v[76:79], v[192:195], v[108:111]
	v_mfma_f32_16x16x32_bf16 v[104:107], v[92:95], v[192:195], v[104:107]
	v_mfma_f32_16x16x32_bf16 v[88:91], v[76:79], v[200:203], v[88:91]
	v_mfma_f32_16x16x32_bf16 v[80:83], v[92:95], v[200:203], v[80:83]
	s_setprio 0
	s_setprio 1
	v_mfma_f32_16x16x32_bf16 v[132:135], v[144:147], v[160:163], v[132:135]
	v_mfma_f32_16x16x32_bf16 v[128:131], v[152:155], v[160:163], v[128:131]
	v_mfma_f32_16x16x32_bf16 v[116:119], v[144:147], v[168:171], v[116:119]
	v_mfma_f32_16x16x32_bf16 v[112:115], v[152:155], v[168:171], v[112:115]
	v_mfma_f32_16x16x32_bf16 v[100:103], v[144:147], v[188:191], v[100:103]
	v_mfma_f32_16x16x32_bf16 v[96:99], v[152:155], v[188:191], v[96:99]
	v_mfma_f32_16x16x32_bf16 v[68:71], v[144:147], v[196:199], v[68:71]
	v_mfma_f32_16x16x32_bf16 v[64:67], v[152:155], v[196:199], v[64:67]
	v_mfma_f32_16x16x32_bf16 v[132:135], v[148:151], v[164:167], v[132:135]
	v_mfma_f32_16x16x32_bf16 v[128:131], v[156:159], v[164:167], v[128:131]
	v_mfma_f32_16x16x32_bf16 v[116:119], v[148:151], v[184:187], v[116:119]
	v_mfma_f32_16x16x32_bf16 v[112:115], v[156:159], v[184:187], v[112:115]
	v_mfma_f32_16x16x32_bf16 v[100:103], v[148:151], v[192:195], v[100:103]
	v_mfma_f32_16x16x32_bf16 v[96:99], v[156:159], v[192:195], v[96:99]
	v_mfma_f32_16x16x32_bf16 v[68:71], v[148:151], v[200:203], v[68:71]
	v_mfma_f32_16x16x32_bf16 v[64:67], v[156:159], v[200:203], v[64:67]
	s_barrier
	s_setprio 0
	ds_read_b128 v[160:163], v207 offset:16384
	ds_read_b128 v[164:167], v207 offset:17408
	ds_read_b128 v[168:171], v207 offset:18432
	ds_read_b128 v[184:187], v207 offset:19456
	ds_read_b128 v[188:191], v207 offset:20480
	ds_read_b128 v[192:195], v207 offset:21504
	ds_read_b128 v[196:199], v207 offset:22528
	ds_read_b128 v[200:203], v207 offset:23552
	s_mov_b32 m0, s31
	s_add_u32 s0, s48, 0x4000
	global_load_lds_dwordx4 v174, s[48:49]
	s_mov_b32 m0, s43
	s_addc_u32 s1, s49, 0
	global_load_lds_dwordx4 v178, s[48:49]
	s_mov_b32 m0, s53
	s_nop 0
	global_load_lds_dwordx4 v174, s[0:1]
	s_mov_b32 m0, s54
	s_nop 0
	global_load_lds_dwordx4 v178, s[0:1]
	s_mov_b32 m0, s56
	s_nop 0
	global_load_lds_dwordx4 v172, s[50:51]
	s_mov_b32 m0, s57
	s_nop 0
	global_load_lds_dwordx4 v176, s[50:51]
	s_waitcnt vmcnt(8)
	s_waitcnt lgkmcnt(0)
	s_setprio 1
	s_barrier
	v_mfma_f32_16x16x32_bf16 v[60:63], v[72:75], v[160:163], v[60:63]
	v_mfma_f32_16x16x32_bf16 v[56:59], v[84:87], v[160:163], v[56:59]
	v_mfma_f32_16x16x32_bf16 v[44:47], v[72:75], v[168:171], v[44:47]
	v_mfma_f32_16x16x32_bf16 v[40:43], v[84:87], v[168:171], v[40:43]
	v_mfma_f32_16x16x32_bf16 v[28:31], v[72:75], v[188:191], v[28:31]
	v_mfma_f32_16x16x32_bf16 v[24:27], v[84:87], v[188:191], v[24:27]
	v_mfma_f32_16x16x32_bf16 v[12:15], v[72:75], v[196:199], v[12:15]
	v_mfma_f32_16x16x32_bf16 v[8:11], v[84:87], v[196:199], v[8:11]
	v_mfma_f32_16x16x32_bf16 v[60:63], v[76:79], v[164:167], v[60:63]
	v_mfma_f32_16x16x32_bf16 v[56:59], v[92:95], v[164:167], v[56:59]
	v_mfma_f32_16x16x32_bf16 v[44:47], v[76:79], v[184:187], v[44:47]
	v_mfma_f32_16x16x32_bf16 v[40:43], v[92:95], v[184:187], v[40:43]
	v_mfma_f32_16x16x32_bf16 v[28:31], v[76:79], v[192:195], v[28:31]
	v_mfma_f32_16x16x32_bf16 v[24:27], v[92:95], v[192:195], v[24:27]
	v_mfma_f32_16x16x32_bf16 v[12:15], v[76:79], v[200:203], v[12:15]
	v_mfma_f32_16x16x32_bf16 v[8:11], v[92:95], v[200:203], v[8:11]
	s_setprio 0
	s_setprio 1
	v_mfma_f32_16x16x32_bf16 v[52:55], v[144:147], v[160:163], v[52:55]
	v_mfma_f32_16x16x32_bf16 v[48:51], v[152:155], v[160:163], v[48:51]
	v_mfma_f32_16x16x32_bf16 v[36:39], v[144:147], v[168:171], v[36:39]
	v_mfma_f32_16x16x32_bf16 v[32:35], v[152:155], v[168:171], v[32:35]
	v_mfma_f32_16x16x32_bf16 v[20:23], v[144:147], v[188:191], v[20:23]
	v_mfma_f32_16x16x32_bf16 v[16:19], v[152:155], v[188:191], v[16:19]
	v_mfma_f32_16x16x32_bf16 v[4:7], v[144:147], v[196:199], v[4:7]
	v_mfma_f32_16x16x32_bf16 v[0:3], v[152:155], v[196:199], v[0:3]
	v_mfma_f32_16x16x32_bf16 v[52:55], v[148:151], v[164:167], v[52:55]
	v_mfma_f32_16x16x32_bf16 v[48:51], v[156:159], v[164:167], v[48:51]
	v_mfma_f32_16x16x32_bf16 v[36:39], v[148:151], v[184:187], v[36:39]
	v_mfma_f32_16x16x32_bf16 v[32:35], v[156:159], v[184:187], v[32:35]
	v_mfma_f32_16x16x32_bf16 v[20:23], v[148:151], v[192:195], v[20:23]
	v_mfma_f32_16x16x32_bf16 v[16:19], v[156:159], v[192:195], v[16:19]
	v_mfma_f32_16x16x32_bf16 v[4:7], v[148:151], v[200:203], v[4:7]
	v_mfma_f32_16x16x32_bf16 v[0:3], v[156:159], v[200:203], v[0:3]
	s_barrier
	s_setprio 0
	v_add_u32_e32 v92, s64, v206
	v_add_u32_e32 v156, s69, v206
	ds_read_b128 v[72:75], v92
	ds_read_b128 v[76:79], v92 offset:1024
	ds_read_b128 v[84:87], v92 offset:2048
	ds_read_b128 v[92:95], v92 offset:3072
	ds_read_b128 v[144:147], v156
	ds_read_b128 v[148:151], v156 offset:1024
	ds_read_b128 v[152:155], v156 offset:2048
	ds_read_b128 v[156:159], v156 offset:3072
	ds_read_b128 v[160:163], v207 offset:32768
	ds_read_b128 v[164:167], v207 offset:33792
	ds_read_b128 v[168:171], v207 offset:34816
	ds_read_b128 v[184:187], v207 offset:35840
	ds_read_b128 v[188:191], v207 offset:36864
	ds_read_b128 v[192:195], v207 offset:37888
	ds_read_b128 v[196:199], v207 offset:38912
	ds_read_b128 v[200:203], v207 offset:39936
	s_add_u32 s0, s50, 0x4000
	s_addc_u32 s1, s51, 0
	s_mov_b32 m0, s58
	s_nop 0
	global_load_lds_dwordx4 v172, s[0:1]
	s_mov_b32 m0, s59
	s_nop 0
	global_load_lds_dwordx4 v176, s[0:1]
	s_waitcnt vmcnt(8)
	s_waitcnt lgkmcnt(0)
	s_setprio 1
	s_barrier
	v_mfma_f32_16x16x32_bf16 v[140:143], v[72:75], v[160:163], v[140:143]
	v_mfma_f32_16x16x32_bf16 v[136:139], v[84:87], v[160:163], v[136:139]
	v_mfma_f32_16x16x32_bf16 v[124:127], v[72:75], v[168:171], v[124:127]
	v_mfma_f32_16x16x32_bf16 v[120:123], v[84:87], v[168:171], v[120:123]
	v_mfma_f32_16x16x32_bf16 v[108:111], v[72:75], v[188:191], v[108:111]
	v_mfma_f32_16x16x32_bf16 v[104:107], v[84:87], v[188:191], v[104:107]
	v_mfma_f32_16x16x32_bf16 v[88:91], v[72:75], v[196:199], v[88:91]
	v_mfma_f32_16x16x32_bf16 v[80:83], v[84:87], v[196:199], v[80:83]
	v_mfma_f32_16x16x32_bf16 v[140:143], v[76:79], v[164:167], v[140:143]
	v_mfma_f32_16x16x32_bf16 v[136:139], v[92:95], v[164:167], v[136:139]
	v_mfma_f32_16x16x32_bf16 v[124:127], v[76:79], v[184:187], v[124:127]
	v_mfma_f32_16x16x32_bf16 v[120:123], v[92:95], v[184:187], v[120:123]
	v_mfma_f32_16x16x32_bf16 v[108:111], v[76:79], v[192:195], v[108:111]
	v_mfma_f32_16x16x32_bf16 v[104:107], v[92:95], v[192:195], v[104:107]
	v_mfma_f32_16x16x32_bf16 v[88:91], v[76:79], v[200:203], v[88:91]
	v_mfma_f32_16x16x32_bf16 v[80:83], v[92:95], v[200:203], v[80:83]
	s_setprio 0
	s_setprio 1
	v_mfma_f32_16x16x32_bf16 v[132:135], v[144:147], v[160:163], v[132:135]
	v_mfma_f32_16x16x32_bf16 v[128:131], v[152:155], v[160:163], v[128:131]
	v_mfma_f32_16x16x32_bf16 v[116:119], v[144:147], v[168:171], v[116:119]
	v_mfma_f32_16x16x32_bf16 v[112:115], v[152:155], v[168:171], v[112:115]
	v_mfma_f32_16x16x32_bf16 v[100:103], v[144:147], v[188:191], v[100:103]
	v_mfma_f32_16x16x32_bf16 v[96:99], v[152:155], v[188:191], v[96:99]
	v_mfma_f32_16x16x32_bf16 v[68:71], v[144:147], v[196:199], v[68:71]
	v_mfma_f32_16x16x32_bf16 v[64:67], v[152:155], v[196:199], v[64:67]
	v_mfma_f32_16x16x32_bf16 v[132:135], v[148:151], v[164:167], v[132:135]
	v_mfma_f32_16x16x32_bf16 v[128:131], v[156:159], v[164:167], v[128:131]
	v_mfma_f32_16x16x32_bf16 v[116:119], v[148:151], v[184:187], v[116:119]
	v_mfma_f32_16x16x32_bf16 v[112:115], v[156:159], v[184:187], v[112:115]
	v_mfma_f32_16x16x32_bf16 v[100:103], v[148:151], v[192:195], v[100:103]
	v_mfma_f32_16x16x32_bf16 v[96:99], v[156:159], v[192:195], v[96:99]
	v_mfma_f32_16x16x32_bf16 v[68:71], v[148:151], v[200:203], v[68:71]
	v_mfma_f32_16x16x32_bf16 v[64:67], v[156:159], v[200:203], v[64:67]
	s_barrier
	s_setprio 0
	ds_read_b128 v[160:163], v207 offset:49152
	ds_read_b128 v[164:167], v207 offset:50176
	ds_read_b128 v[168:171], v207 offset:51200
	ds_read_b128 v[184:187], v207 offset:52224
	ds_read_b128 v[188:191], v207 offset:53248
	ds_read_b128 v[192:195], v207 offset:54272
	ds_read_b128 v[196:199], v207 offset:55296
	ds_read_b128 v[200:203], v207 offset:56320
	s_add_u32 s0, s48, 0x8000
	s_addc_u32 s1, s49, 0
	s_mov_b32 m0, s65
	s_nop 0
	global_load_lds_dwordx4 v174, s[0:1]
	s_mov_b32 m0, s66
	s_nop 0
	global_load_lds_dwordx4 v178, s[0:1]
	s_add_u32 s0, s48, 0xc000
	s_addc_u32 s1, s49, 0
	s_mov_b32 m0, s70
	s_nop 0
	global_load_lds_dwordx4 v174, s[0:1]
	s_mov_b32 m0, s71
	s_nop 0
	global_load_lds_dwordx4 v178, s[0:1]
	s_mov_b32 m0, s67
	s_nop 0
	global_load_lds_dwordx4 v172, s[46:47]
	s_mov_b32 m0, s68
	s_nop 0
	global_load_lds_dwordx4 v176, s[46:47]
	s_waitcnt vmcnt(8)
	s_waitcnt lgkmcnt(0)
	s_setprio 1
	s_barrier
	v_mfma_f32_16x16x32_bf16 v[60:63], v[72:75], v[160:163], v[60:63]
	v_mfma_f32_16x16x32_bf16 v[56:59], v[84:87], v[160:163], v[56:59]
	v_mfma_f32_16x16x32_bf16 v[44:47], v[72:75], v[168:171], v[44:47]
	v_mfma_f32_16x16x32_bf16 v[40:43], v[84:87], v[168:171], v[40:43]
	v_mfma_f32_16x16x32_bf16 v[28:31], v[72:75], v[188:191], v[28:31]
	v_mfma_f32_16x16x32_bf16 v[24:27], v[84:87], v[188:191], v[24:27]
	v_mfma_f32_16x16x32_bf16 v[12:15], v[72:75], v[196:199], v[12:15]
	v_mfma_f32_16x16x32_bf16 v[8:11], v[84:87], v[196:199], v[8:11]
	v_mfma_f32_16x16x32_bf16 v[60:63], v[76:79], v[164:167], v[60:63]
	v_mfma_f32_16x16x32_bf16 v[56:59], v[92:95], v[164:167], v[56:59]
	v_mfma_f32_16x16x32_bf16 v[44:47], v[76:79], v[184:187], v[44:47]
	v_mfma_f32_16x16x32_bf16 v[40:43], v[92:95], v[184:187], v[40:43]
	v_mfma_f32_16x16x32_bf16 v[28:31], v[76:79], v[192:195], v[28:31]
	v_mfma_f32_16x16x32_bf16 v[24:27], v[92:95], v[192:195], v[24:27]
	v_mfma_f32_16x16x32_bf16 v[12:15], v[76:79], v[200:203], v[12:15]
	v_mfma_f32_16x16x32_bf16 v[8:11], v[92:95], v[200:203], v[8:11]
	s_setprio 0
	s_setprio 1
	v_mfma_f32_16x16x32_bf16 v[52:55], v[144:147], v[160:163], v[52:55]
	v_mfma_f32_16x16x32_bf16 v[48:51], v[152:155], v[160:163], v[48:51]
	v_mfma_f32_16x16x32_bf16 v[36:39], v[144:147], v[168:171], v[36:39]
	v_mfma_f32_16x16x32_bf16 v[32:35], v[152:155], v[168:171], v[32:35]
	v_mfma_f32_16x16x32_bf16 v[20:23], v[144:147], v[188:191], v[20:23]
	v_mfma_f32_16x16x32_bf16 v[16:19], v[152:155], v[188:191], v[16:19]
	v_mfma_f32_16x16x32_bf16 v[4:7], v[144:147], v[196:199], v[4:7]
	v_mfma_f32_16x16x32_bf16 v[0:3], v[152:155], v[196:199], v[0:3]
	v_mfma_f32_16x16x32_bf16 v[52:55], v[148:151], v[164:167], v[52:55]
	v_mfma_f32_16x16x32_bf16 v[48:51], v[156:159], v[164:167], v[48:51]
	v_mfma_f32_16x16x32_bf16 v[36:39], v[148:151], v[184:187], v[36:39]
	v_mfma_f32_16x16x32_bf16 v[32:35], v[156:159], v[184:187], v[32:35]
	v_mfma_f32_16x16x32_bf16 v[20:23], v[148:151], v[192:195], v[20:23]
	v_mfma_f32_16x16x32_bf16 v[16:19], v[156:159], v[192:195], v[16:19]
	v_mfma_f32_16x16x32_bf16 v[4:7], v[148:151], v[200:203], v[4:7]
	v_mfma_f32_16x16x32_bf16 v[0:3], v[156:159], v[200:203], v[0:3]
	s_barrier
	s_setprio 0
	s_add_i32 s76, s76, 2
	s_add_u32 s74, s74, 0x10000
	s_addc_u32 s75, s75, 0
	s_cmpk_gt_u32 s76, 0x7d
	s_mov_b64 s[0:1], s[44:45]
	s_cbranch_scc0 .LBB0_1248
	s_and_b64 vcc, exec, s[22:23]
	s_cbranch_vccz .LBB0_1251
	s_barrier
